# k_gcn gather loop: index loads issued before row loads, loop-top wait vmcnt(4), row wait moved to accumulate as vmcnt(8) (two row batches in flight)
# speedup vs baseline: 1.0060x; 1.0047x over previous
.LBB2_9:
	v_add_lshl_u32 v68, v50, s33, 2
	v_subrev_u32_e32 v69, s33, v53
	global_load_dword v64, v68, s[22:23]
	global_load_dword v55, v68, s[22:23] offset:4
	global_load_dword v66, v68, s[22:23] offset:8
	global_load_dword v65, v68, s[22:23] offset:12
	v_lshl_or_b32 v34, v36, 8, v54
	buffer_load_dwordx4 v[34:37], v34, s[24:27], 0 offen
	v_lshl_or_b32 v38, v38, 8, v54
	buffer_load_dwordx4 v[38:41], v38, s[24:27], 0 offen
	v_lshl_or_b32 v42, v42, 8, v54
	buffer_load_dwordx4 v[42:45], v42, s[24:27], 0 offen
	v_lshl_or_b32 v46, v46, 8, v54
	buffer_load_dwordx4 v[46:49], v46, s[24:27], 0 offen
.Lkg_A:
	s_waitcnt vmcnt(4)
	s_cmp_ge_i32 s33, s31
	s_cbranch_scc1 .Lkg_finA
	v_cmp_lt_i32_e64 s[34:35], 0, v69
	v_cmp_lt_i32_e64 s[36:37], 1, v69
	v_cmp_lt_i32_e64 s[38:39], 2, v69
	v_cmp_lt_i32_e64 s[40:41], 3, v69
	v_cndmask_b32_e64 v72, v70, v64, s[34:35]
	v_cndmask_b32_e64 v76, v70, v55, s[36:37]
	v_cndmask_b32_e64 v86, v70, v66, s[38:39]
	v_cndmask_b32_e64 v90, v70, v65, s[40:41]
	s_add_i32 s33, s33, 4
	v_add_lshl_u32 v68, v50, s33, 2
	v_subrev_u32_e32 v69, s33, v53
	global_load_dword v64, v68, s[22:23]
	global_load_dword v55, v68, s[22:23] offset:4
	global_load_dword v66, v68, s[22:23] offset:8
	global_load_dword v65, v68, s[22:23] offset:12
	v_lshl_or_b32 v72, v72, 8, v54
	buffer_load_dwordx4 v[72:75], v72, s[24:27], 0 offen
	v_lshl_or_b32 v76, v76, 8, v54
	buffer_load_dwordx4 v[76:79], v76, s[24:27], 0 offen
	v_lshl_or_b32 v86, v86, 8, v54
	buffer_load_dwordx4 v[86:89], v86, s[24:27], 0 offen
	v_lshl_or_b32 v90, v90, 8, v54
	buffer_load_dwordx4 v[90:93], v90, s[24:27], 0 offen
	s_waitcnt vmcnt(8)
	v_fma_mix_f32 v62, v34, 1.0, v62 op_sel_hi:[1,0,0]
	v_fma_mix_f32 v63, v34, 1.0, v63 op_sel:[1,0,0] op_sel_hi:[1,0,0]
	v_fma_mix_f32 v60, v35, 1.0, v60 op_sel_hi:[1,0,0]
	v_fma_mix_f32 v61, v35, 1.0, v61 op_sel:[1,0,0] op_sel_hi:[1,0,0]
	v_fma_mix_f32 v58, v36, 1.0, v58 op_sel_hi:[1,0,0]
	v_fma_mix_f32 v59, v36, 1.0, v59 op_sel:[1,0,0] op_sel_hi:[1,0,0]
	v_fma_mix_f32 v56, v37, 1.0, v56 op_sel_hi:[1,0,0]
	v_fma_mix_f32 v57, v37, 1.0, v57 op_sel:[1,0,0] op_sel_hi:[1,0,0]
	v_fma_mix_f32 v62, v38, 1.0, v62 op_sel_hi:[1,0,0]
	v_fma_mix_f32 v63, v38, 1.0, v63 op_sel:[1,0,0] op_sel_hi:[1,0,0]
	v_fma_mix_f32 v60, v39, 1.0, v60 op_sel_hi:[1,0,0]
	v_fma_mix_f32 v61, v39, 1.0, v61 op_sel:[1,0,0] op_sel_hi:[1,0,0]
	v_fma_mix_f32 v58, v40, 1.0, v58 op_sel_hi:[1,0,0]
	v_fma_mix_f32 v59, v40, 1.0, v59 op_sel:[1,0,0] op_sel_hi:[1,0,0]
	v_fma_mix_f32 v56, v41, 1.0, v56 op_sel_hi:[1,0,0]
	v_fma_mix_f32 v57, v41, 1.0, v57 op_sel:[1,0,0] op_sel_hi:[1,0,0]
	v_fma_mix_f32 v62, v42, 1.0, v62 op_sel_hi:[1,0,0]
	v_fma_mix_f32 v63, v42, 1.0, v63 op_sel:[1,0,0] op_sel_hi:[1,0,0]
	v_fma_mix_f32 v60, v43, 1.0, v60 op_sel_hi:[1,0,0]
	v_fma_mix_f32 v61, v43, 1.0, v61 op_sel:[1,0,0] op_sel_hi:[1,0,0]
	v_fma_mix_f32 v58, v44, 1.0, v58 op_sel_hi:[1,0,0]
	v_fma_mix_f32 v59, v44, 1.0, v59 op_sel:[1,0,0] op_sel_hi:[1,0,0]
	v_fma_mix_f32 v56, v45, 1.0, v56 op_sel_hi:[1,0,0]
	v_fma_mix_f32 v57, v45, 1.0, v57 op_sel:[1,0,0] op_sel_hi:[1,0,0]
	v_fma_mix_f32 v62, v46, 1.0, v62 op_sel_hi:[1,0,0]
	v_fma_mix_f32 v63, v46, 1.0, v63 op_sel:[1,0,0] op_sel_hi:[1,0,0]
	v_fma_mix_f32 v60, v47, 1.0, v60 op_sel_hi:[1,0,0]
	v_fma_mix_f32 v61, v47, 1.0, v61 op_sel:[1,0,0] op_sel_hi:[1,0,0]
	v_fma_mix_f32 v58, v48, 1.0, v58 op_sel_hi:[1,0,0]
	v_fma_mix_f32 v59, v48, 1.0, v59 op_sel:[1,0,0] op_sel_hi:[1,0,0]
	v_fma_mix_f32 v56, v49, 1.0, v56 op_sel_hi:[1,0,0]
	v_fma_mix_f32 v57, v49, 1.0, v57 op_sel:[1,0,0] op_sel_hi:[1,0,0]
.Lkg_B:
	s_waitcnt vmcnt(4)
	s_cmp_ge_i32 s33, s31
	s_cbranch_scc1 .Lkg_finB
	v_cmp_lt_i32_e64 s[34:35], 0, v69
	v_cmp_lt_i32_e64 s[36:37], 1, v69
	v_cmp_lt_i32_e64 s[38:39], 2, v69
	v_cmp_lt_i32_e64 s[40:41], 3, v69
	v_cndmask_b32_e64 v34, v70, v64, s[34:35]
	v_cndmask_b32_e64 v38, v70, v55, s[36:37]
	v_cndmask_b32_e64 v42, v70, v66, s[38:39]
	v_cndmask_b32_e64 v46, v70, v65, s[40:41]
	s_add_i32 s33, s33, 4
	v_add_lshl_u32 v68, v50, s33, 2
	v_subrev_u32_e32 v69, s33, v53
	global_load_dword v64, v68, s[22:23]
	global_load_dword v55, v68, s[22:23] offset:4
	global_load_dword v66, v68, s[22:23] offset:8
	global_load_dword v65, v68, s[22:23] offset:12
	v_lshl_or_b32 v34, v34, 8, v54
	buffer_load_dwordx4 v[34:37], v34, s[24:27], 0 offen
	v_lshl_or_b32 v38, v38, 8, v54
	buffer_load_dwordx4 v[38:41], v38, s[24:27], 0 offen
	v_lshl_or_b32 v42, v42, 8, v54
	buffer_load_dwordx4 v[42:45], v42, s[24:27], 0 offen
	v_lshl_or_b32 v46, v46, 8, v54
	buffer_load_dwordx4 v[46:49], v46, s[24:27], 0 offen
	s_waitcnt vmcnt(8)
	v_fma_mix_f32 v62, v72, 1.0, v62 op_sel_hi:[1,0,0]
	v_fma_mix_f32 v63, v72, 1.0, v63 op_sel:[1,0,0] op_sel_hi:[1,0,0]
	v_fma_mix_f32 v60, v73, 1.0, v60 op_sel_hi:[1,0,0]
	v_fma_mix_f32 v61, v73, 1.0, v61 op_sel:[1,0,0] op_sel_hi:[1,0,0]
	v_fma_mix_f32 v58, v74, 1.0, v58 op_sel_hi:[1,0,0]
	v_fma_mix_f32 v59, v74, 1.0, v59 op_sel:[1,0,0] op_sel_hi:[1,0,0]
	v_fma_mix_f32 v56, v75, 1.0, v56 op_sel_hi:[1,0,0]
	v_fma_mix_f32 v57, v75, 1.0, v57 op_sel:[1,0,0] op_sel_hi:[1,0,0]
	v_fma_mix_f32 v62, v76, 1.0, v62 op_sel_hi:[1,0,0]
	v_fma_mix_f32 v63, v76, 1.0, v63 op_sel:[1,0,0] op_sel_hi:[1,0,0]
	v_fma_mix_f32 v60, v77, 1.0, v60 op_sel_hi:[1,0,0]
	v_fma_mix_f32 v61, v77, 1.0, v61 op_sel:[1,0,0] op_sel_hi:[1,0,0]
	v_fma_mix_f32 v58, v78, 1.0, v58 op_sel_hi:[1,0,0]
	v_fma_mix_f32 v59, v78, 1.0, v59 op_sel:[1,0,0] op_sel_hi:[1,0,0]
	v_fma_mix_f32 v56, v79, 1.0, v56 op_sel_hi:[1,0,0]
	v_fma_mix_f32 v57, v79, 1.0, v57 op_sel:[1,0,0] op_sel_hi:[1,0,0]
	v_fma_mix_f32 v62, v86, 1.0, v62 op_sel_hi:[1,0,0]
	v_fma_mix_f32 v63, v86, 1.0, v63 op_sel:[1,0,0] op_sel_hi:[1,0,0]
	v_fma_mix_f32 v60, v87, 1.0, v60 op_sel_hi:[1,0,0]
	v_fma_mix_f32 v61, v87, 1.0, v61 op_sel:[1,0,0] op_sel_hi:[1,0,0]
	v_fma_mix_f32 v58, v88, 1.0, v58 op_sel_hi:[1,0,0]
	v_fma_mix_f32 v59, v88, 1.0, v59 op_sel:[1,0,0] op_sel_hi:[1,0,0]
	v_fma_mix_f32 v56, v89, 1.0, v56 op_sel_hi:[1,0,0]
	v_fma_mix_f32 v57, v89, 1.0, v57 op_sel:[1,0,0] op_sel_hi:[1,0,0]
	v_fma_mix_f32 v62, v90, 1.0, v62 op_sel_hi:[1,0,0]
	v_fma_mix_f32 v63, v90, 1.0, v63 op_sel:[1,0,0] op_sel_hi:[1,0,0]
	v_fma_mix_f32 v60, v91, 1.0, v60 op_sel_hi:[1,0,0]
	v_fma_mix_f32 v61, v91, 1.0, v61 op_sel:[1,0,0] op_sel_hi:[1,0,0]
	v_fma_mix_f32 v58, v92, 1.0, v58 op_sel_hi:[1,0,0]
	v_fma_mix_f32 v59, v92, 1.0, v59 op_sel:[1,0,0] op_sel_hi:[1,0,0]
	v_fma_mix_f32 v56, v93, 1.0, v56 op_sel_hi:[1,0,0]
	v_fma_mix_f32 v57, v93, 1.0, v57 op_sel:[1,0,0] op_sel_hi:[1,0,0]
	s_branch .Lkg_A
.Lkg_finA:
	s_waitcnt vmcnt(0)
	v_fma_mix_f32 v62, v34, 1.0, v62 op_sel_hi:[1,0,0]
	v_fma_mix_f32 v63, v34, 1.0, v63 op_sel:[1,0,0] op_sel_hi:[1,0,0]
	v_fma_mix_f32 v60, v35, 1.0, v60 op_sel_hi:[1,0,0]
	v_fma_mix_f32 v61, v35, 1.0, v61 op_sel:[1,0,0] op_sel_hi:[1,0,0]
	v_fma_mix_f32 v58, v36, 1.0, v58 op_sel_hi:[1,0,0]
	v_fma_mix_f32 v59, v36, 1.0, v59 op_sel:[1,0,0] op_sel_hi:[1,0,0]
	v_fma_mix_f32 v56, v37, 1.0, v56 op_sel_hi:[1,0,0]
	v_fma_mix_f32 v57, v37, 1.0, v57 op_sel:[1,0,0] op_sel_hi:[1,0,0]
	v_fma_mix_f32 v62, v38, 1.0, v62 op_sel_hi:[1,0,0]
	v_fma_mix_f32 v63, v38, 1.0, v63 op_sel:[1,0,0] op_sel_hi:[1,0,0]
	v_fma_mix_f32 v60, v39, 1.0, v60 op_sel_hi:[1,0,0]
	v_fma_mix_f32 v61, v39, 1.0, v61 op_sel:[1,0,0] op_sel_hi:[1,0,0]
	v_fma_mix_f32 v58, v40, 1.0, v58 op_sel_hi:[1,0,0]
	v_fma_mix_f32 v59, v40, 1.0, v59 op_sel:[1,0,0] op_sel_hi:[1,0,0]
	v_fma_mix_f32 v56, v41, 1.0, v56 op_sel_hi:[1,0,0]
	v_fma_mix_f32 v57, v41, 1.0, v57 op_sel:[1,0,0] op_sel_hi:[1,0,0]
	v_fma_mix_f32 v62, v42, 1.0, v62 op_sel_hi:[1,0,0]
	v_fma_mix_f32 v63, v42, 1.0, v63 op_sel:[1,0,0] op_sel_hi:[1,0,0]
	v_fma_mix_f32 v60, v43, 1.0, v60 op_sel_hi:[1,0,0]
	v_fma_mix_f32 v61, v43, 1.0, v61 op_sel:[1,0,0] op_sel_hi:[1,0,0]
	v_fma_mix_f32 v58, v44, 1.0, v58 op_sel_hi:[1,0,0]
	v_fma_mix_f32 v59, v44, 1.0, v59 op_sel:[1,0,0] op_sel_hi:[1,0,0]
	v_fma_mix_f32 v56, v45, 1.0, v56 op_sel_hi:[1,0,0]
	v_fma_mix_f32 v57, v45, 1.0, v57 op_sel:[1,0,0] op_sel_hi:[1,0,0]
	v_fma_mix_f32 v62, v46, 1.0, v62 op_sel_hi:[1,0,0]
	v_fma_mix_f32 v63, v46, 1.0, v63 op_sel:[1,0,0] op_sel_hi:[1,0,0]
	v_fma_mix_f32 v60, v47, 1.0, v60 op_sel_hi:[1,0,0]
	v_fma_mix_f32 v61, v47, 1.0, v61 op_sel:[1,0,0] op_sel_hi:[1,0,0]
	v_fma_mix_f32 v58, v48, 1.0, v58 op_sel_hi:[1,0,0]
	v_fma_mix_f32 v59, v48, 1.0, v59 op_sel:[1,0,0] op_sel_hi:[1,0,0]
	v_fma_mix_f32 v56, v49, 1.0, v56 op_sel_hi:[1,0,0]
	v_fma_mix_f32 v57, v49, 1.0, v57 op_sel:[1,0,0] op_sel_hi:[1,0,0]
	s_branch .LBB2_19
.Lkg_finB:
	s_waitcnt vmcnt(0)
	v_fma_mix_f32 v62, v72, 1.0, v62 op_sel_hi:[1,0,0]
	v_fma_mix_f32 v63, v72, 1.0, v63 op_sel:[1,0,0] op_sel_hi:[1,0,0]
	v_fma_mix_f32 v60, v73, 1.0, v60 op_sel_hi:[1,0,0]
	v_fma_mix_f32 v61, v73, 1.0, v61 op_sel:[1,0,0] op_sel_hi:[1,0,0]
	v_fma_mix_f32 v58, v74, 1.0, v58 op_sel_hi:[1,0,0]
	v_fma_mix_f32 v59, v74, 1.0, v59 op_sel:[1,0,0] op_sel_hi:[1,0,0]
	v_fma_mix_f32 v56, v75, 1.0, v56 op_sel_hi:[1,0,0]
	v_fma_mix_f32 v57, v75, 1.0, v57 op_sel:[1,0,0] op_sel_hi:[1,0,0]
	v_fma_mix_f32 v62, v76, 1.0, v62 op_sel_hi:[1,0,0]
	v_fma_mix_f32 v63, v76, 1.0, v63 op_sel:[1,0,0] op_sel_hi:[1,0,0]
	v_fma_mix_f32 v60, v77, 1.0, v60 op_sel_hi:[1,0,0]
	v_fma_mix_f32 v61, v77, 1.0, v61 op_sel:[1,0,0] op_sel_hi:[1,0,0]
	v_fma_mix_f32 v58, v78, 1.0, v58 op_sel_hi:[1,0,0]
	v_fma_mix_f32 v59, v78, 1.0, v59 op_sel:[1,0,0] op_sel_hi:[1,0,0]
	v_fma_mix_f32 v56, v79, 1.0, v56 op_sel_hi:[1,0,0]
	v_fma_mix_f32 v57, v79, 1.0, v57 op_sel:[1,0,0] op_sel_hi:[1,0,0]
	v_fma_mix_f32 v62, v86, 1.0, v62 op_sel_hi:[1,0,0]
	v_fma_mix_f32 v63, v86, 1.0, v63 op_sel:[1,0,0] op_sel_hi:[1,0,0]
	v_fma_mix_f32 v60, v87, 1.0, v60 op_sel_hi:[1,0,0]
	v_fma_mix_f32 v61, v87, 1.0, v61 op_sel:[1,0,0] op_sel_hi:[1,0,0]
	v_fma_mix_f32 v58, v88, 1.0, v58 op_sel_hi:[1,0,0]
	v_fma_mix_f32 v59, v88, 1.0, v59 op_sel:[1,0,0] op_sel_hi:[1,0,0]
	v_fma_mix_f32 v56, v89, 1.0, v56 op_sel_hi:[1,0,0]
	v_fma_mix_f32 v57, v89, 1.0, v57 op_sel:[1,0,0] op_sel_hi:[1,0,0]
	v_fma_mix_f32 v62, v90, 1.0, v62 op_sel_hi:[1,0,0]
	v_fma_mix_f32 v63, v90, 1.0, v63 op_sel:[1,0,0] op_sel_hi:[1,0,0]
	v_fma_mix_f32 v60, v91, 1.0, v60 op_sel_hi:[1,0,0]
	v_fma_mix_f32 v61, v91, 1.0, v61 op_sel:[1,0,0] op_sel_hi:[1,0,0]
	v_fma_mix_f32 v58, v92, 1.0, v58 op_sel_hi:[1,0,0]
	v_fma_mix_f32 v59, v92, 1.0, v59 op_sel:[1,0,0] op_sel_hi:[1,0,0]
	v_fma_mix_f32 v56, v93, 1.0, v56 op_sel_hi:[1,0,0]
	v_fma_mix_f32 v57, v93, 1.0, v57 op_sel:[1,0,0] op_sel_hi:[1,0,0]
